# mixer chunk loop: static s_setprio 1 for waves 0-3 instead (per-half comparison)
# baseline (speedup 1.0000x reference)
.LBB0_464:
	s_ashr_i32 s8, s24, 2
	s_add_i32 s24, s8, s78
	s_lshl_b32 s8, s79, 7
	s_and_b64 s[78:79], s[76:77], exec
	s_movk_i32 s9, 0x1500
	s_cselect_b32 s9, s9, 0x1800
	s_and_b64 s[6:7], exec, s[6:7]
	s_cselect_b32 s6, 0x900, s9
	s_lshl_b32 s2, s2, 6
	s_and_b32 s40, s2, 64
	s_add_i32 s7, s81, s8
	s_or_b32 s78, s7, s40
	s_ashr_i32 s7, s5, 31
	s_lshr_b32 s7, s7, 30
	s_add_i32 s7, s5, s7
	s_and_b32 s7, s7, 0x1ffffc
	s_sub_i32 s5, s5, s7
	s_lshl_b32 s84, s5, 11
	v_cndmask_b32_e64 v3, v111, v110, s[76:77]
	v_add_u32_e32 v3, s84, v3
	s_add_i32 s2, s80, s8
	v_mad_i64_i32 v[4:5], s[80:81], v3, s20, v[38:39]
	s_add_i32 s6, s6, s8
	s_mov_b32 s7, s3
	s_lshl_b64 s[80:81], s[2:3], 1
	s_mov_b32 m0, s19
	v_lshl_add_u64 v[6:7], v[4:5], 0, s[80:81]
	s_lshl_b64 s[6:7], s[6:7], 1
	v_cndmask_b32_e64 v3, v113, v112, s[76:77]
	s_waitcnt vmcnt(0) lgkmcnt(0)
	s_barrier
	global_load_lds_dwordx4 v[6:7], off
	v_lshl_add_u64 v[4:5], v[4:5], 0, s[6:7]
	s_mov_b32 m0, s82
	v_add_u32_e32 v3, s84, v3
	global_load_lds_dwordx4 v[4:5], off
	v_mad_i64_i32 v[4:5], s[86:87], v3, s20, v[38:39]
	s_add_i32 s85, s92, 0x1b600
	v_lshl_add_u64 v[6:7], v[4:5], 0, s[80:81]
	s_mov_b32 m0, s85
	s_add_i32 s86, s92, 0x1f600
	global_load_lds_dwordx4 v[6:7], off
	v_lshl_add_u64 v[4:5], v[4:5], 0, s[6:7]
	s_mov_b32 m0, s86
	v_cndmask_b32_e64 v3, v101, v100, s[76:77]
	global_load_lds_dwordx4 v[4:5], off
	v_add_u32_e32 v3, s84, v3
	v_mov_b64_e32 v[4:5], s[26:27]
	s_mov_b32 s79, s3
	v_mad_i64_i32 v[4:5], vcc, v3, s20, v[4:5]
	s_lshl_b64 s[78:79], s[78:79], 1
	s_add_i32 s87, s16, 0
	v_lshl_add_u64 v[4:5], v[4:5], 0, s[78:79]
	v_mov_b32_e32 v45, v195
	s_add_i32 s87, s87, 0x23600
	v_lshl_add_u64 v[4:5], v[4:5], 0, v[44:45]
	s_mov_b32 m0, s87
	v_mul_f32_e32 v144, 0x42800000, v2
	global_load_lds_dwordx4 v[4:5], off
	v_mul_f32_e32 v2, 0x42000000, v2
	v_exp_f32_e32 v18, v2
	s_ashr_i32 s9, s8, 31
	s_waitcnt vmcnt(0)
	s_lshl_b32 s2, s4, 13
	v_mad_i64_i32 v[2:3], s[4:5], s24, v242, v[42:43]
	v_lshl_add_u64 v[2:3], s[8:9], 1, v[2:3]
	s_lshl_b32 s4, s40, 1
	s_mov_b32 s5, s3
	v_mov_b32_e32 v22, 0
	v_lshl_add_u64 v[52:53], v[40:41], 0, s[78:79]
	v_sub_f32_e32 v45, 1.0, v140
	v_sub_f32_e32 v143, 1.0, v139
	v_lshl_add_u64 v[54:55], v[2:3], 0, s[4:5]
	v_mov_b32_e32 v47, v46
	s_mov_b32 s24, 0
	v_mov_b32_e32 v19, v18
	v_mov_b32_e32 v20, v18
	v_mov_b32_e32 v21, v18
	s_mov_b32 s4, 0
	v_mov_b32_e32 v23, v22
	v_mov_b32_e32 v24, v22
	v_mov_b32_e32 v25, v22
	v_mov_b32_e32 v26, v22
	v_mov_b32_e32 v27, v22
	v_mov_b32_e32 v28, v22
	v_mov_b32_e32 v29, v22
	v_mov_b32_e32 v30, v22
	v_mov_b32_e32 v31, v22
	v_mov_b32_e32 v32, v22
	v_mov_b32_e32 v33, v22
	v_mov_b32_e32 v34, v22
	v_mov_b32_e32 v35, v22
	v_mov_b32_e32 v36, v22
	v_mov_b32_e32 v37, v22
	v_readfirstlane_b32 s100, v0
	s_nop 3
	s_lshr_b32 s100, s100, 6
	s_cmp_ge_u32 s100, 4
	s_cbranch_scc1 .Lmx_prio_done
	s_setprio 1
